# C1 + MoE epilogues: row->token (gate/up) and routing-weight (down) loads of a unit issued at the top of the unit instead of behind its main loop
# baseline (speedup 1.0000x reference)
.LBB0_1398:
	s_lshl_b32 s2, s42, 8
	v_add_u32_e32 v244, s2, v200
	v_ashrrev_i32_e32 v245, 31, v244
	v_lshl_add_u64 v[244:245], v[244:245], 2, s[0:1]
	global_load_dword v236, v[244:245], off
	global_load_dword v237, v[244:245], off offset:64
	global_load_dword v238, v[244:245], off offset:128
	global_load_dword v239, v[244:245], off offset:192
	global_load_dword v240, v[244:245], off offset:512
	global_load_dword v241, v[244:245], off offset:576
	global_load_dword v242, v[244:245], off offset:640
	global_load_dword v243, v[244:245], off offset:704
	s_add_i32 s80, s80, 1
	s_mul_i32 s2, s80, s29
	s_mul_hi_u32 s3, s80, s28
	s_add_i32 s3, s3, s2
	s_mul_i32 s2, s80, s28
	s_add_u32 s8, s2, s94
	s_addc_u32 s9, s3, s95
	v_cmp_ge_i64_e32 vcc, s[8:9], v[136:137]
	v_cmp_lt_i64_e64 s[10:11], s[8:9], v[136:137]
	s_cbranch_vccnz .LBB0_1402
	s_ashr_i32 s2, s9, 31
	s_lshr_b32 s2, s2, 30
	s_add_u32 s44, s8, s2
	s_addc_u32 s45, s9, 0
	s_ashr_i64 s[58:59], s[44:45], 2
	s_mov_b64 s[60:61], 0
	s_and_saveexec_b64 s[62:63], s[6:7]
	s_cbranch_execz .LBB0_1401
	ds_read_b32 v2, v202
	s_waitcnt lgkmcnt(0)
	v_cmp_ge_i32_e32 vcc, s58, v2
	s_and_b64 s[60:61], vcc, exec

.LBB0_1408:
	s_ashr_i32 s65, s64, 31
	s_lshl_b64 s[10:11], s[64:65], 12
	s_add_u32 s2, s23, s10
	s_addc_u32 s3, s25, s11
	s_lshl_b32 s10, s82, 8
	s_ashr_i32 s11, s10, 31
	s_lshl_b64 s[10:11], s[10:11], 2
	s_add_u32 s2, s2, s10
	s_addc_u32 s3, s3, s11
	s_add_u32 s10, s2, s78
	v_cvt_f32_i32_e32 v163, v124
	v_mov_b32_e32 v124, 0
	s_addc_u32 s11, s3, 0
	s_lshl_b32 s2, s42, 8
	v_cvt_f32_i32_e32 v171, v128
	v_add3_u32 v180, s2, v200, v124
	v_cvt_f32_i32_e32 v179, v126
	v_ashrrev_i32_e32 v181, 31, v180
	v_add_u32_e32 v150, 16, v180
	v_add_u32_e32 v138, 32, v180
	v_add_u32_e32 v128, 48, v180
	v_add_u32_e32 v126, 0x80, v180
	v_add_u32_e32 v124, 0x90, v180
	v_cvt_f32_i32_e32 v167, v129
	v_cvt_f32_i32_e32 v175, v127
	v_cvt_f32_i32_e32 v159, v125
	v_mov_b32_e32 v134, 0
	v_lshl_add_u64 v[140:141], v[180:181], 2, s[0:1]
	v_ashrrev_i32_e32 v151, 31, v150
	v_ashrrev_i32_e32 v139, 31, v138
	v_ashrrev_i32_e32 v129, 31, v128
	v_ashrrev_i32_e32 v127, 31, v126
	v_ashrrev_i32_e32 v125, 31, v124
	v_lshl_add_u64 v[142:143], v[150:151], 2, s[0:1]
	v_lshl_add_u64 v[144:145], v[138:139], 2, s[0:1]
	v_lshl_add_u64 v[146:147], v[128:129], 2, s[0:1]
	v_lshl_add_u64 v[148:149], v[126:127], 2, s[0:1]
	v_lshl_add_u64 v[152:153], v[124:125], 2, s[0:1]
	v_mov_b32_e32 v212, v236
	v_mov_b32_e32 v214, v237
	v_mov_b32_e32 v216, v238
	v_mov_b32_e32 v218, v239
	v_mov_b32_e32 v220, v240
	v_mov_b32_e32 v222, v241
	v_cvt_f32_i32_e32 v170, v96
	v_cvt_f32_i32_e32 v178, v94
	v_add_u32_e32 v96, 0xa0, v180
	v_add_u32_e32 v94, 0xb0, v180
	v_cvt_f32_i32_e32 v166, v97
	v_cvt_f32_i32_e32 v174, v95
	v_ashrrev_i32_e32 v97, 31, v96
	v_ashrrev_i32_e32 v95, 31, v94
	v_cvt_f32_i32_e32 v185, v121
	v_cvt_f32_i32_e32 v189, v119
	v_cvt_f32_i32_e32 v177, v115
	v_cvt_f32_i32_e32 v155, v113
	v_cvt_f32_i32_e32 v157, v112
	v_cvt_f32_i32_e32 v145, v109
	v_cvt_f32_i32_e32 v149, v107
	v_cvt_f32_i32_e32 v153, v106
	v_cvt_f32_i32_e32 v121, v105
	v_cvt_f32_i32_e32 v107, v101
	v_cvt_f32_i32_e32 v113, v100
	v_cvt_f32_i32_e32 v115, v99
	v_cvt_f32_i32_e32 v119, v98
	v_lshl_add_u64 v[98:99], v[96:97], 2, s[0:1]
	v_lshl_add_u64 v[100:101], v[94:95], 2, s[0:1]
	v_cvt_f32_i32_e32 v106, v69
	v_cvt_f32_i32_e32 v112, v68
	v_cvt_f32_i32_e32 v105, v39
	v_cvt_f32_i32_e32 v109, v38
	v_cvt_f32_i32_e32 v195, v122
	v_cvt_f32_i32_e32 v187, v120
	v_cvt_f32_i32_e32 v173, v116
	v_mov_b32_e32 v116, v242
	v_mov_b32_e32 v224, v243
	v_cvt_f32_i32_e32 v160, v79
	v_cvt_f32_i32_e32 v164, v78
	v_cvt_f32_i32_e32 v148, v75
	v_cvt_f32_i32_e32 v152, v74
	v_cvt_f32_i32_e32 v120, v73
	v_cvt_f32_i32_e32 v122, v72
	v_cvt_f32_i32_e32 v142, v70
	v_cvt_f32_i32_e32 v99, v41
	v_cvt_f32_i32_e32 v101, v40
	v_add_lshl_u32 v70, v134, v199, 3
	v_cvt_f32_i32_e32 v154, v81
	v_cvt_f32_i32_e32 v156, v80
	v_cvt_f32_i32_e32 v144, v77
	v_cvt_f32_i32_e32 v146, v76
	v_cvt_f32_i32_e32 v140, v71
	v_ashrrev_i32_e32 v71, 31, v70
	v_cvt_f32_i32_e32 v191, v118
	v_cvt_f32_i32_e32 v183, v114
	v_cvt_f32_i32_e32 v114, v67
	v_cvt_f32_i32_e32 v118, v66
	v_lshl_add_u64 v[66:67], v[70:71], 2, s[10:11]
	v_cvt_f32_i32_e32 v182, v82
	v_cvt_f32_i32_e32 v82, v2
	v_cvt_f32_i32_e32 v162, v92
	v_cvt_f32_i32_e32 v194, v90
	v_cvt_f32_i32_e32 v90, v7
	v_cvt_f32_i32_e32 v92, v6
	v_cvt_f32_i32_e32 v169, v117
	v_cvt_f32_i32_e32 v141, v103
	v_cvt_f32_i32_e32 v188, v87
	v_cvt_f32_i32_e32 v87, v49
	v_cvt_f32_i32_e32 v103, v48
	v_cvt_f32_i32_e32 v186, v88
	v_cvt_f32_i32_e32 v172, v84
	v_cvt_f32_i32_e32 v84, v9
	v_cvt_f32_i32_e32 v88, v8
	v_cvt_f32_i32_e32 v165, v110
	v_cvt_f32_i32_e32 v110, v11
	v_cvt_f32_i32_e32 v190, v86
	v_cvt_f32_i32_e32 v86, v13
	v_cvt_f32_i32_e32 v193, v123
	v_cvt_f32_i32_e32 v123, v104
	v_cvt_f32_i32_e32 v104, v15
	v_ashrrev_i32_e32 v213, 31, v212
	v_ashrrev_i32_e32 v215, 31, v214
	v_ashrrev_i32_e32 v217, 31, v216
	v_ashrrev_i32_e32 v219, 31, v218
	v_lshlrev_b64 v[38:39], 2, v[212:213]
	v_lshlrev_b64 v[68:69], 2, v[214:215]
	v_ashrrev_i32_e32 v221, 31, v220
	v_ashrrev_i32_e32 v223, 31, v222
	v_lshl_add_u64 v[40:41], s[52:53], 0, v[38:39]
	v_lshl_add_u64 v[38:39], s[12:13], 0, v[38:39]
	v_lshl_add_u64 v[72:73], s[52:53], 0, v[68:69]
	v_lshl_add_u64 v[68:69], s[12:13], 0, v[68:69]
	v_lshlrev_b64 v[74:75], 2, v[216:217]
	v_lshlrev_b64 v[78:79], 2, v[218:219]
	v_lshl_add_u64 v[76:77], s[52:53], 0, v[74:75]
	v_lshl_add_u64 v[74:75], s[12:13], 0, v[74:75]
	v_lshl_add_u64 v[80:81], s[52:53], 0, v[78:79]
	v_lshl_add_u64 v[78:79], s[12:13], 0, v[78:79]
	global_load_dword v134, v[40:41], off
	global_load_dword v211, v[38:39], off
	global_load_dword v226, v[72:73], off
	global_load_dword v227, v[68:69], off
	global_load_dword v228, v[76:77], off
	global_load_dword v229, v[74:75], off
	global_load_dword v230, v[80:81], off
	global_load_dword v231, v[78:79], off
	v_lshlrev_b64 v[38:39], 2, v[220:221]
	v_lshlrev_b64 v[68:69], 2, v[222:223]
	v_lshl_add_u64 v[40:41], s[52:53], 0, v[38:39]
	v_lshl_add_u64 v[38:39], s[12:13], 0, v[38:39]
	v_lshl_add_u64 v[72:73], s[52:53], 0, v[68:69]
	v_lshl_add_u64 v[68:69], s[12:13], 0, v[68:69]
	global_load_dword v220, v[40:41], off
	global_load_dword v221, v[38:39], off
	global_load_dword v222, v[72:73], off
	global_load_dword v223, v[68:69], off
	global_load_dwordx4 v[212:215], v[66:67], off offset:528
	global_load_dwordx4 v[216:219], v[66:67], off offset:512
	s_nop 0
	global_load_dwordx4 v[38:41], v[66:67], off offset:16
	s_nop 0
	global_load_dwordx4 v[66:69], v[66:67], off
	v_cvt_f32_i32_e32 v79, v36
	v_cvt_f32_i32_e32 v36, v56
	v_cvt_f32_i32_e32 v76, v5
	v_cvt_f32_i32_e32 v78, v4
	v_cvt_f32_i32_e32 v80, v3
	v_cvt_f32_i32_e32 v75, v30
	v_cvt_f32_i32_e32 v30, v59
	v_cvt_f32_i32_e32 v98, v17
	v_cvt_f32_i32_e32 v168, v85
	v_ashrrev_i32_e32 v117, 31, v116
	v_lshlrev_b64 v[48:49], 2, v[116:117]
	v_cvt_f32_i32_e32 v116, v10
	v_ashrrev_i32_e32 v225, 31, v224
	v_lshl_add_u64 v[72:73], s[52:53], 0, v[48:49]
	v_lshl_add_u64 v[48:49], s[12:13], 0, v[48:49]
	global_load_dword v232, v[72:73], off
	global_load_dword v233, v[48:49], off
	v_lshlrev_b64 v[48:49], 2, v[224:225]
	v_lshl_add_u64 v[72:73], s[52:53], 0, v[48:49]
	v_lshl_add_u64 v[48:49], s[12:13], 0, v[48:49]
	global_load_dword v224, v[72:73], off
	global_load_dword v225, v[48:49], off
	v_cvt_f32_i32_e32 v49, v32
	v_cvt_f32_i32_e32 v32, v58
	v_cvt_f32_i32_e32 v85, v45
	v_cvt_f32_i32_e32 v77, v37
	v_cvt_f32_i32_e32 v37, v28
	v_cvt_f32_i32_e32 v45, v26
	v_cvt_f32_i32_e32 v26, v61
	v_cvt_f32_i32_e32 v28, v60
	v_cvt_f32_i32_e32 v192, v91
	v_cvt_f32_i32_e32 v72, v51
	v_cvt_f32_i32_e32 v91, v43
	v_cvt_f32_i32_e32 v81, v35
	v_cvt_f32_i32_e32 v35, v29
	v_cvt_f32_i32_e32 v43, v27
	v_cvt_f32_i32_e32 v27, v25
	v_cvt_f32_i32_e32 v29, v24
	v_cvt_f32_i32_e32 v25, v18
	v_cvt_f32_i32_e32 v18, v63
	v_cvt_f32_i32_e32 v24, v62
	v_cvt_f32_i32_e32 v158, v93
	v_cvt_f32_i32_e32 v117, v46
	v_cvt_f32_i32_e32 v46, v53
	v_cvt_f32_i32_e32 v176, v83
	v_cvt_f32_i32_e32 v93, v42
	v_cvt_f32_i32_e32 v83, v34
	v_cvt_f32_i32_e32 v34, v57
	v_cvt_f32_i32_e32 v42, v55
	v_cvt_f32_i32_e32 v184, v89
	v_cvt_f32_i32_e32 v89, v44
	v_cvt_f32_i32_e32 v44, v54
	v_readlane_b32 s2, v255, 20
	v_readlane_b32 s3, v255, 21
	s_lshl_b32 s10, s82, 7
	s_ashr_i32 s11, s10, 31
	v_cvt_f32_i32_e32 v48, v52
	v_cvt_f32_i32_e32 v161, v111
	v_cvt_f32_i32_e32 v147, v108
	v_cvt_f32_i32_e32 v143, v102
	v_cvt_f32_i32_e32 v74, v50
	v_cvt_f32_i32_e32 v108, v14
	v_cvt_f32_i32_e32 v100, v16
	v_cvt_f32_i32_e32 v111, v47
	v_cvt_f32_i32_e32 v102, v12
	v_cvt_f32_i32_e32 v73, v31
	v_cvt_f32_i32_e32 v47, v33
	v_cvt_f32_i32_e32 v33, v22
	s_waitcnt vmcnt(18)
	v_mul_f32_e32 v56, v134, v211
	v_pk_mul_f32 v[2:3], v[178:179], v[56:57] op_sel_hi:[1,0]
	v_pk_mul_f32 v[58:59], v[166:167], v[56:57] op_sel_hi:[1,0]
	v_pk_mul_f32 v[60:61], v[194:195], v[56:57] op_sel_hi:[1,0]
	s_waitcnt vmcnt(16)
	v_mul_f32_e32 v54, v226, v227
	s_waitcnt vmcnt(14)
	v_mul_f32_e32 v52, v228, v229
	s_waitcnt vmcnt(12)
	v_mul_f32_e32 v50, v230, v231
	s_waitcnt vmcnt(10)
	v_mul_f32_e32 v16, v220, v221
	v_cvt_f32_i32_e32 v31, v23
	s_waitcnt vmcnt(8)
	v_mul_f32_e32 v14, v222, v223
	v_cvt_f32_i32_e32 v19, v19
	s_waitcnt vmcnt(6)
	v_mov_b32_e32 v4, v216
	v_cvt_f32_i32_e32 v23, v20
	s_waitcnt vmcnt(4)
	v_mov_b32_e32 v5, v66
	v_pk_mul_f32 v[6:7], v[4:5], v[2:3]
	v_mov_b32_e32 v66, v217
	v_mul_f32_e32 v2, 0xbfb8aa3b, v7
	v_exp_f32_e32 v10, v2
	v_pk_mul_f32 v[2:3], v[174:175], v[56:57] op_sel_hi:[1,0]
	v_cvt_f32_i32_e32 v22, v64
	v_pk_mul_f32 v[8:9], v[66:67], v[2:3]
	v_add_f32_e32 v3, 1.0, v10
	v_mul_f32_e32 v2, 0xbfb8aa3b, v9
	v_exp_f32_e32 v2, v2
	v_rcp_f32_e32 v3, v3
	v_cvt_f32_i32_e32 v21, v21
	v_cvt_f32_i32_e32 v20, v65
	v_add_f32_e32 v2, 1.0, v2
	v_rcp_f32_e32 v10, v2
	v_mul_f32_e32 v3, v7, v3
	v_mul_f32_e32 v3, v6, v3
	v_mov_b32_e32 v6, v218
	v_mul_f32_e32 v9, v9, v10
	v_pk_mul_f32 v[10:11], v[170:171], v[56:57] op_sel_hi:[1,0]
	v_mov_b32_e32 v7, v68
	v_pk_mul_f32 v[10:11], v[6:7], v[10:11]
	v_mov_b32_e32 v68, v219
	v_mul_f32_e32 v13, 0xbfb8aa3b, v11
	v_pk_mul_f32 v[58:59], v[68:69], v[58:59]
	v_exp_f32_e32 v13, v13
	v_mul_f32_e32 v15, 0xbfb8aa3b, v59
	v_exp_f32_e32 v15, v15
	v_mul_f32_e32 v17, v8, v9
	v_add_f32_e32 v8, 1.0, v13
	v_rcp_f32_e32 v13, v8
	v_add_f32_e32 v8, 1.0, v15
	v_rcp_f32_e32 v15, v8
	v_mov_b32_e32 v8, v212
	v_mov_b32_e32 v9, v38
	v_pk_mul_f32 v[60:61], v[8:9], v[60:61]
	v_mul_f32_e32 v11, v11, v13
	v_mul_f32_e32 v38, 0xbfb8aa3b, v61
	v_exp_f32_e32 v38, v38
	v_mul_f32_e32 v13, v10, v11
	v_mul_f32_e32 v15, v59, v15
	v_mul_f32_e32 v15, v58, v15
	v_add_f32_e32 v10, 1.0, v38
	v_rcp_f32_e32 v51, v10
	v_pk_mul_f32 v[10:11], v[192:193], v[56:57] op_sel_hi:[1,0]
	v_mov_b32_e32 v38, v213
	v_pk_mul_f32 v[62:63], v[38:39], v[10:11]
	v_mul_f32_e32 v11, v61, v51
	v_mul_f32_e32 v10, 0xbfb8aa3b, v63
	v_exp_f32_e32 v10, v10
	v_mul_f32_e32 v51, v60, v11
	v_pk_mul_f32 v[58:59], v[162:163], v[56:57] op_sel_hi:[1,0]
	v_mov_b32_e32 v11, v40
	v_add_f32_e32 v10, 1.0, v10
	v_rcp_f32_e32 v53, v10
	v_mov_b32_e32 v10, v214
	v_pk_mul_f32 v[58:59], v[10:11], v[58:59]
	v_pk_mul_f32 v[56:57], v[158:159], v[56:57] op_sel_hi:[1,0]
	v_mul_f32_e32 v40, 0xbfb8aa3b, v59
	v_exp_f32_e32 v55, v40
	v_mov_b32_e32 v40, v215
	v_pk_mul_f32 v[56:57], v[40:41], v[56:57]
	v_mul_f32_e32 v3, 0x41000000, v3
	v_mul_f32_e32 v60, 0xbfb8aa3b, v57
	v_exp_f32_e32 v60, v60
	v_add_f32_e32 v55, 1.0, v55
	v_rcp_f32_e32 v55, v55
	v_mul_f32_e32 v17, 0x41000000, v17
	v_add_f32_e32 v60, 1.0, v60
	v_rcp_f32_e32 v60, v60
	v_mul_f32_e32 v55, v59, v55
	v_mul_f32_e32 v55, v58, v55
	v_med3_f32 v3, v3, s79, v206
	v_mul_f32_e32 v57, v57, v60
	v_mul_f32_e32 v58, v56, v57
	v_med3_f32 v17, v17, s79, v206
	v_mov_b32_e32 v56, 0
	v_cvt_pk_fp8_f32 v56, v3, v17
	v_mul_f32_e32 v53, v63, v53
	v_mul_f32_e32 v13, 0x41000000, v13
	v_mul_f32_e32 v3, 0x41000000, v15
	v_mul_f32_e32 v53, v62, v53
	v_med3_f32 v13, v13, s79, v206
	v_med3_f32 v3, v3, s79, v206
	v_cvt_pk_fp8_f32 v56, v13, v3 op_sel:[0,0,1]
	v_mul_f32_e32 v3, 0x41000000, v51
	v_mul_f32_e32 v13, 0x41000000, v53
	v_med3_f32 v3, v3, s79, v206
	v_med3_f32 v13, v13, s79, v206
	v_mov_b32_e32 v57, 0
	v_cvt_pk_fp8_f32 v57, v3, v13
	v_mul_f32_e32 v15, 0x41000000, v55
	v_mul_f32_e32 v3, 0x41000000, v58
	v_pk_mul_f32 v[60:61], v[190:191], v[54:55] op_sel_hi:[1,0]
	v_med3_f32 v13, v15, s79, v206
	v_med3_f32 v3, v3, s79, v206
	v_pk_mul_f32 v[60:61], v[4:5], v[60:61]
	v_cvt_pk_fp8_f32 v57, v13, v3 op_sel:[0,0,1]
	v_mul_f32_e32 v3, 0xbfb8aa3b, v61
	v_lshlrev_b64 v[58:59], 9, v[180:181]
	v_exp_f32_e32 v3, v3
	v_lshl_add_u64 v[58:59], s[2:3], 0, v[58:59]
	v_lshl_add_u64 v[58:59], v[58:59], 0, s[10:11]
	v_lshl_add_u64 v[58:59], v[58:59], 0, s[30:31]
	v_lshl_add_u64 v[58:59], v[58:59], 0, v[70:71]
	v_add_f32_e32 v3, 1.0, v3
	v_rcp_f32_e32 v3, v3
	global_store_dwordx2 v[58:59], v[56:57], off
	v_pk_mul_f32 v[56:57], v[186:187], v[54:55] op_sel_hi:[1,0]
	v_pk_mul_f32 v[58:59], v[184:185], v[54:55] op_sel_hi:[1,0]
	v_pk_mul_f32 v[56:57], v[6:7], v[56:57]
	v_pk_mul_f32 v[58:59], v[68:69], v[58:59]
	v_mul_f32_e32 v15, 0xbfb8aa3b, v57
	v_exp_f32_e32 v15, v15
	v_mul_f32_e32 v3, v61, v3
	v_mul_f32_e32 v17, 0xbfb8aa3b, v59
	v_mul_f32_e32 v3, v60, v3
	v_exp_f32_e32 v17, v17
	v_pk_mul_f32 v[60:61], v[182:183], v[54:55] op_sel_hi:[1,0]
	v_add_f32_e32 v15, 1.0, v15
	v_pk_mul_f32 v[60:61], v[8:9], v[60:61]
	v_rcp_f32_e32 v15, v15
	v_mul_f32_e32 v51, 0xbfb8aa3b, v61
	v_exp_f32_e32 v51, v51
	v_add_f32_e32 v17, 1.0, v17
	v_rcp_f32_e32 v17, v17
	v_mul_f32_e32 v15, v57, v15
	v_add_f32_e32 v51, 1.0, v51
	v_mul_f32_e32 v15, v56, v15
	v_rcp_f32_e32 v51, v51
	v_pk_mul_f32 v[56:57], v[176:177], v[54:55] op_sel_hi:[1,0]
	v_mul_f32_e32 v17, v59, v17
	v_pk_mul_f32 v[56:57], v[38:39], v[56:57]
	v_mul_f32_e32 v17, v58, v17
	v_mul_f32_e32 v53, 0xbfb8aa3b, v57
	v_pk_mul_f32 v[58:59], v[172:173], v[54:55] op_sel_hi:[1,0]
	v_pk_mul_f32 v[62:63], v[188:189], v[54:55] op_sel_hi:[1,0]
	v_exp_f32_e32 v53, v53
	v_pk_mul_f32 v[58:59], v[10:11], v[58:59]
	v_pk_mul_f32 v[62:63], v[66:67], v[62:63]
	v_mul_f32_e32 v51, v61, v51
	v_mul_f32_e32 v55, 0xbfb8aa3b, v59
	v_mul_f32_e32 v13, 0xbfb8aa3b, v63
	v_mul_f32_e32 v51, v60, v51
	v_exp_f32_e32 v60, v55
	v_pk_mul_f32 v[54:55], v[168:169], v[54:55] op_sel_hi:[1,0]
	v_exp_f32_e32 v13, v13
	v_pk_mul_f32 v[54:55], v[40:41], v[54:55]
	v_add_f32_e32 v53, 1.0, v53
	v_mul_f32_e32 v61, 0xbfb8aa3b, v55
	v_rcp_f32_e32 v53, v53
	v_exp_f32_e32 v61, v61
	v_add_f32_e32 v13, 1.0, v13
	v_rcp_f32_e32 v13, v13
	v_mul_f32_e32 v53, v57, v53
	v_add_f32_e32 v57, 1.0, v60
	v_add_f32_e32 v60, 1.0, v61
	v_rcp_f32_e32 v60, v60
	v_rcp_f32_e32 v57, v57
	v_mul_f32_e32 v13, v63, v13
	v_mul_f32_e32 v13, v62, v13
	v_mul_f32_e32 v55, v55, v60
	v_mul_f32_e32 v3, 0x41000000, v3
	v_mul_f32_e32 v13, 0x41000000, v13
	v_mul_f32_e32 v53, v56, v53
	v_mul_f32_e32 v56, v59, v57
	v_mul_f32_e32 v57, v54, v55
	v_med3_f32 v3, v3, s79, v206
	v_med3_f32 v13, v13, s79, v206
	v_mov_b32_e32 v54, 0
	v_cvt_pk_fp8_f32 v54, v3, v13
	v_mul_f32_e32 v15, 0x41000000, v15
	v_mul_f32_e32 v3, 0x41000000, v17
	v_med3_f32 v13, v15, s79, v206
	v_med3_f32 v3, v3, s79, v206
	v_cvt_pk_fp8_f32 v54, v13, v3 op_sel:[0,0,1]
	v_mul_f32_e32 v3, 0x41000000, v51
	v_mul_f32_e32 v13, 0x41000000, v53
	v_med3_f32 v3, v3, s79, v206
	v_med3_f32 v13, v13, s79, v206
	v_mov_b32_e32 v55, 0
	v_cvt_pk_fp8_f32 v55, v3, v13
	v_mul_f32_e32 v56, v58, v56
	v_mul_f32_e32 v15, 0x41000000, v56
	v_mul_f32_e32 v3, 0x41000000, v57
	v_med3_f32 v13, v15, s79, v206
	v_med3_f32 v3, v3, s79, v206
	v_lshlrev_b64 v[56:57], 9, v[150:151]
	v_cvt_pk_fp8_f32 v55, v13, v3 op_sel:[0,0,1]
	v_lshl_add_u64 v[56:57], s[2:3], 0, v[56:57]
	v_lshl_add_u64 v[56:57], v[56:57], 0, s[10:11]
	v_pk_mul_f32 v[58:59], v[164:165], v[52:53] op_sel_hi:[1,0]
	v_lshl_add_u64 v[56:57], v[56:57], 0, s[30:31]
	v_pk_mul_f32 v[58:59], v[4:5], v[58:59]
	v_lshl_add_u64 v[56:57], v[56:57], 0, v[70:71]
	v_mul_f32_e32 v3, 0xbfb8aa3b, v59
	v_exp_f32_e32 v3, v3
	global_store_dwordx2 v[56:57], v[54:55], off
	v_pk_mul_f32 v[54:55], v[156:157], v[52:53] op_sel_hi:[1,0]
	v_pk_mul_f32 v[56:57], v[154:155], v[52:53] op_sel_hi:[1,0]
	v_pk_mul_f32 v[54:55], v[6:7], v[54:55]
	v_add_f32_e32 v3, 1.0, v3
	v_mul_f32_e32 v15, 0xbfb8aa3b, v55
	v_exp_f32_e32 v15, v15
	v_rcp_f32_e32 v3, v3
	v_pk_mul_f32 v[56:57], v[68:69], v[56:57]
	v_pk_mul_f32 v[60:61], v[160:161], v[52:53] op_sel_hi:[1,0]
	v_add_f32_e32 v15, 1.0, v15
	v_rcp_f32_e32 v15, v15
	v_mul_f32_e32 v3, v59, v3
	v_mul_f32_e32 v3, v58, v3
	v_mul_f32_e32 v17, 0xbfb8aa3b, v57
	v_pk_mul_f32 v[58:59], v[152:153], v[52:53] op_sel_hi:[1,0]
	v_exp_f32_e32 v17, v17
	v_pk_mul_f32 v[58:59], v[8:9], v[58:59]
	v_mul_f32_e32 v15, v55, v15
	v_mul_f32_e32 v51, 0xbfb8aa3b, v59
	v_exp_f32_e32 v51, v51
	v_mul_f32_e32 v15, v54, v15
	v_pk_mul_f32 v[54:55], v[148:149], v[52:53] op_sel_hi:[1,0]
	v_pk_mul_f32 v[60:61], v[66:67], v[60:61]
	v_pk_mul_f32 v[54:55], v[38:39], v[54:55]
	v_mul_f32_e32 v13, 0xbfb8aa3b, v61
	v_add_f32_e32 v17, 1.0, v17
	v_mul_f32_e32 v53, 0xbfb8aa3b, v55
	v_exp_f32_e32 v13, v13
	v_rcp_f32_e32 v17, v17
	v_exp_f32_e32 v53, v53
	v_add_f32_e32 v51, 1.0, v51
	v_rcp_f32_e32 v51, v51
	v_add_f32_e32 v13, 1.0, v13
	v_mul_f32_e32 v17, v57, v17
	v_add_f32_e32 v53, 1.0, v53
	v_rcp_f32_e32 v13, v13
	v_mul_f32_e32 v17, v56, v17
	v_pk_mul_f32 v[56:57], v[146:147], v[52:53] op_sel_hi:[1,0]
	v_mul_f32_e32 v51, v59, v51
	v_pk_mul_f32 v[56:57], v[10:11], v[56:57]
	v_mul_f32_e32 v51, v58, v51
	v_rcp_f32_e32 v58, v53
	v_mul_f32_e32 v53, 0xbfb8aa3b, v57
	v_exp_f32_e32 v59, v53
	v_pk_mul_f32 v[52:53], v[144:145], v[52:53] op_sel_hi:[1,0]
	v_mul_f32_e32 v13, v61, v13
	v_pk_mul_f32 v[52:53], v[40:41], v[52:53]
	v_mul_f32_e32 v13, v60, v13
	v_mul_f32_e32 v60, 0xbfb8aa3b, v53
	v_exp_f32_e32 v60, v60
	v_mul_f32_e32 v55, v55, v58
	v_add_f32_e32 v58, 1.0, v59
	v_rcp_f32_e32 v58, v58
	v_add_f32_e32 v59, 1.0, v60
	v_rcp_f32_e32 v59, v59
	v_mul_f32_e32 v54, v54, v55
	v_mul_f32_e32 v55, v57, v58
	v_mul_f32_e32 v3, 0x41000000, v3
	v_mul_f32_e32 v53, v53, v59
	v_mul_f32_e32 v13, 0x41000000, v13
	v_mul_f32_e32 v55, v56, v55
	v_mul_f32_e32 v56, v52, v53
	v_med3_f32 v3, v3, s79, v206
	v_med3_f32 v13, v13, s79, v206
	v_mov_b32_e32 v52, 0
	v_cvt_pk_fp8_f32 v52, v3, v13
	v_mul_f32_e32 v15, 0x41000000, v15
	v_mul_f32_e32 v3, 0x41000000, v17
	v_med3_f32 v13, v15, s79, v206
	v_med3_f32 v3, v3, s79, v206
	v_cvt_pk_fp8_f32 v52, v13, v3 op_sel:[0,0,1]
	v_mul_f32_e32 v3, 0x41000000, v51
	v_mul_f32_e32 v13, 0x41000000, v54
	v_med3_f32 v3, v3, s79, v206
	v_med3_f32 v13, v13, s79, v206
	v_mov_b32_e32 v53, 0
	v_cvt_pk_fp8_f32 v53, v3, v13
	v_mul_f32_e32 v15, 0x41000000, v55
	v_mul_f32_e32 v3, 0x41000000, v56
	v_pk_mul_f32 v[56:57], v[142:143], v[50:51] op_sel_hi:[1,0]
	v_med3_f32 v13, v15, s79, v206
	v_med3_f32 v3, v3, s79, v206
	v_pk_mul_f32 v[56:57], v[4:5], v[56:57]
	v_cvt_pk_fp8_f32 v53, v13, v3 op_sel:[0,0,1]
	v_mul_f32_e32 v3, 0xbfb8aa3b, v57
	v_exp_f32_e32 v3, v3
	v_lshlrev_b64 v[54:55], 9, v[138:139]
	v_lshl_add_u64 v[54:55], s[2:3], 0, v[54:55]
	v_lshl_add_u64 v[54:55], v[54:55], 0, s[10:11]
	v_add_f32_e32 v3, 1.0, v3
	v_rcp_f32_e32 v3, v3
	v_lshl_add_u64 v[54:55], v[54:55], 0, s[30:31]
	v_lshl_add_u64 v[54:55], v[54:55], 0, v[70:71]
	global_store_dwordx2 v[54:55], v[52:53], off
	v_mul_f32_e32 v3, v57, v3
	v_pk_mul_f32 v[52:53], v[122:123], v[50:51] op_sel_hi:[1,0]
	v_mul_f32_e32 v3, v56, v3
	v_pk_mul_f32 v[52:53], v[6:7], v[52:53]
	v_pk_mul_f32 v[56:57], v[118:119], v[50:51] op_sel_hi:[1,0]
	v_mul_f32_e32 v15, 0xbfb8aa3b, v53
	v_pk_mul_f32 v[56:57], v[8:9], v[56:57]
	v_pk_mul_f32 v[58:59], v[140:141], v[50:51] op_sel_hi:[1,0]
	v_exp_f32_e32 v15, v15
	v_pk_mul_f32 v[54:55], v[120:121], v[50:51] op_sel_hi:[1,0]
	v_mul_f32_e32 v51, 0xbfb8aa3b, v57
	v_pk_mul_f32 v[54:55], v[68:69], v[54:55]
	v_exp_f32_e32 v51, v51
	v_mul_f32_e32 v17, 0xbfb8aa3b, v55
	v_exp_f32_e32 v17, v17
	v_add_f32_e32 v15, 1.0, v15
	v_rcp_f32_e32 v15, v15
	v_add_f32_e32 v51, 1.0, v51
	v_rcp_f32_e32 v51, v51
	v_add_f32_e32 v17, 1.0, v17
	v_rcp_f32_e32 v17, v17
	v_pk_mul_f32 v[58:59], v[66:67], v[58:59]
	v_mul_f32_e32 v15, v53, v15
	v_mul_f32_e32 v13, 0xbfb8aa3b, v59
	v_mul_f32_e32 v15, v52, v15
	v_pk_mul_f32 v[52:53], v[114:115], v[50:51] op_sel_hi:[1,0]
	v_exp_f32_e32 v13, v13
	v_pk_mul_f32 v[52:53], v[38:39], v[52:53]
	v_mul_f32_e32 v17, v55, v17
	v_mul_f32_e32 v55, 0xbfb8aa3b, v53
	v_exp_f32_e32 v55, v55
	v_add_f32_e32 v13, 1.0, v13
	v_rcp_f32_e32 v13, v13
	v_mul_f32_e32 v51, v57, v51
	v_mul_f32_e32 v56, v56, v51
	v_add_f32_e32 v51, 1.0, v55
	v_mul_f32_e32 v17, v54, v17
	v_pk_mul_f32 v[54:55], v[112:113], v[50:51] op_sel_hi:[1,0]
	v_mul_f32_e32 v13, v59, v13
	v_pk_mul_f32 v[54:55], v[10:11], v[54:55]
	v_rcp_f32_e32 v57, v51
	v_mul_f32_e32 v51, 0xbfb8aa3b, v55
	v_mul_f32_e32 v13, v58, v13
	v_exp_f32_e32 v58, v51
	v_pk_mul_f32 v[50:51], v[106:107], v[50:51] op_sel_hi:[1,0]
	v_mul_f32_e32 v53, v53, v57
	v_pk_mul_f32 v[50:51], v[40:41], v[50:51]
	v_add_f32_e32 v57, 1.0, v58
	v_mul_f32_e32 v59, 0xbfb8aa3b, v51
	v_exp_f32_e32 v59, v59
	v_rcp_f32_e32 v57, v57
	v_mul_f32_e32 v52, v52, v53
	v_mul_f32_e32 v3, 0x41000000, v3
	v_add_f32_e32 v58, 1.0, v59
	v_rcp_f32_e32 v58, v58
	v_mul_f32_e32 v53, v55, v57
	v_mul_f32_e32 v13, 0x41000000, v13
	v_mul_f32_e32 v53, v54, v53
	v_mul_f32_e32 v51, v51, v58
	v_mul_f32_e32 v54, v50, v51
	v_med3_f32 v3, v3, s79, v206
	v_med3_f32 v13, v13, s79, v206
	v_mov_b32_e32 v50, 0
	v_cvt_pk_fp8_f32 v50, v3, v13
	v_mul_f32_e32 v15, 0x41000000, v15
	v_mul_f32_e32 v3, 0x41000000, v17
	v_med3_f32 v13, v15, s79, v206
	v_med3_f32 v3, v3, s79, v206
	v_cvt_pk_fp8_f32 v50, v13, v3 op_sel:[0,0,1]
	v_mul_f32_e32 v3, 0x41000000, v56
	v_mul_f32_e32 v13, 0x41000000, v52
	v_med3_f32 v3, v3, s79, v206
	v_med3_f32 v13, v13, s79, v206
	v_mov_b32_e32 v51, 0
	v_cvt_pk_fp8_f32 v51, v3, v13
	v_mul_f32_e32 v15, 0x41000000, v53
	v_mul_f32_e32 v3, 0x41000000, v54
	v_med3_f32 v13, v15, s79, v206
	v_med3_f32 v3, v3, s79, v206
	v_lshlrev_b64 v[52:53], 9, v[128:129]
	v_cvt_pk_fp8_f32 v51, v13, v3 op_sel:[0,0,1]
	v_lshl_add_u64 v[52:53], s[2:3], 0, v[52:53]
	v_lshl_add_u64 v[52:53], v[52:53], 0, s[10:11]
	v_lshl_add_u64 v[52:53], v[52:53], 0, s[30:31]
	v_pk_mul_f32 v[54:55], v[108:109], v[16:17] op_sel_hi:[1,0]
	v_lshl_add_u64 v[52:53], v[52:53], 0, v[70:71]
	v_pk_mul_f32 v[54:55], v[4:5], v[54:55]
	global_store_dwordx2 v[52:53], v[50:51], off
	v_pk_mul_f32 v[52:53], v[98:99], v[16:17] op_sel_hi:[1,0]
	v_mul_f32_e32 v3, 0xbfb8aa3b, v55
	v_pk_mul_f32 v[56:57], v[104:105], v[16:17] op_sel_hi:[1,0]
	v_pk_mul_f32 v[52:53], v[68:69], v[52:53]
	v_exp_f32_e32 v3, v3
	v_pk_mul_f32 v[56:57], v[66:67], v[56:57]
	v_pk_mul_f32 v[50:51], v[100:101], v[16:17] op_sel_hi:[1,0]
	v_mul_f32_e32 v17, 0xbfb8aa3b, v53
	v_mul_f32_e32 v13, 0xbfb8aa3b, v57
	v_exp_f32_e32 v17, v17
	v_exp_f32_e32 v13, v13
	v_add_f32_e32 v3, 1.0, v3
	v_rcp_f32_e32 v3, v3
	v_pk_mul_f32 v[50:51], v[6:7], v[50:51]
	v_add_f32_e32 v17, 1.0, v17
	v_add_f32_e32 v13, 1.0, v13
	v_mul_f32_e32 v15, 0xbfb8aa3b, v51
	v_rcp_f32_e32 v17, v17
	v_rcp_f32_e32 v13, v13
	v_exp_f32_e32 v15, v15
	v_mul_f32_e32 v3, v55, v3
	v_mul_f32_e32 v3, v54, v3
	v_pk_mul_f32 v[54:55], v[116:117], v[16:17] op_sel_hi:[1,0]
	v_mul_f32_e32 v13, v57, v13
	v_add_f32_e32 v15, 1.0, v15
	v_pk_mul_f32 v[54:55], v[8:9], v[54:55]
	v_mul_f32_e32 v13, v56, v13
	v_rcp_f32_e32 v15, v15
	v_mul_f32_e32 v56, 0xbfb8aa3b, v55
	v_exp_f32_e32 v56, v56
	v_mul_f32_e32 v17, v53, v17
	v_mul_f32_e32 v15, v51, v15
	v_mul_f32_e32 v15, v50, v15
	v_add_f32_e32 v50, 1.0, v56
	v_rcp_f32_e32 v53, v50
	v_pk_mul_f32 v[50:51], v[110:111], v[16:17] op_sel_hi:[1,0]
	v_mul_f32_e32 v57, v52, v17
	v_pk_mul_f32 v[50:51], v[38:39], v[50:51]
	v_mul_f32_e32 v17, v55, v53
	v_mul_f32_e32 v56, 0xbfb8aa3b, v51
	v_exp_f32_e32 v56, v56
	v_mul_f32_e32 v54, v54, v17
	v_mul_f32_e32 v3, 0x41000000, v3
	v_mul_f32_e32 v13, 0x41000000, v13
	v_add_f32_e32 v17, 1.0, v56
	v_pk_mul_f32 v[52:53], v[102:103], v[16:17] op_sel_hi:[1,0]
	v_rcp_f32_e32 v55, v17
	v_pk_mul_f32 v[52:53], v[10:11], v[52:53]
	v_med3_f32 v3, v3, s79, v206
	v_mul_f32_e32 v17, 0xbfb8aa3b, v53
	v_exp_f32_e32 v56, v17
	v_pk_mul_f32 v[16:17], v[86:87], v[16:17] op_sel_hi:[1,0]
	v_mul_f32_e32 v51, v51, v55
	v_pk_mul_f32 v[16:17], v[40:41], v[16:17]
	v_add_f32_e32 v55, 1.0, v56
	v_mul_f32_e32 v58, 0xbfb8aa3b, v17
	v_exp_f32_e32 v58, v58
	v_rcp_f32_e32 v55, v55
	v_mul_f32_e32 v50, v50, v51
	v_med3_f32 v13, v13, s79, v206
	v_add_f32_e32 v56, 1.0, v58
	v_rcp_f32_e32 v56, v56
	v_mul_f32_e32 v51, v53, v55
	v_mul_f32_e32 v51, v52, v51
	v_mul_f32_e32 v15, 0x41000000, v15
	v_mul_f32_e32 v17, v17, v56
	v_mul_f32_e32 v52, v16, v17
	v_mov_b32_e32 v16, 0
	v_cvt_pk_fp8_f32 v16, v3, v13
	v_mul_f32_e32 v3, 0x41000000, v57
	v_med3_f32 v13, v15, s79, v206
	v_med3_f32 v3, v3, s79, v206
	v_cvt_pk_fp8_f32 v16, v13, v3 op_sel:[0,0,1]
	v_mul_f32_e32 v3, 0x41000000, v54
	v_mul_f32_e32 v13, 0x41000000, v50
	v_med3_f32 v3, v3, s79, v206
	v_med3_f32 v13, v13, s79, v206
	v_mov_b32_e32 v17, 0
	v_cvt_pk_fp8_f32 v17, v3, v13
	v_mul_f32_e32 v15, 0x41000000, v51
	v_mul_f32_e32 v3, 0x41000000, v52
	v_med3_f32 v13, v15, s79, v206
	v_med3_f32 v3, v3, s79, v206
	v_lshlrev_b64 v[50:51], 9, v[126:127]
	v_cvt_pk_fp8_f32 v17, v13, v3 op_sel:[0,0,1]
	v_lshl_add_u64 v[50:51], s[2:3], 0, v[50:51]
	v_pk_mul_f32 v[52:53], v[92:93], v[14:15] op_sel_hi:[1,0]
	v_lshl_add_u64 v[50:51], v[50:51], 0, s[10:11]
	v_pk_mul_f32 v[52:53], v[4:5], v[52:53]
	v_lshl_add_u64 v[50:51], v[50:51], 0, s[30:31]
	v_mul_f32_e32 v3, 0xbfb8aa3b, v53
	v_exp_f32_e32 v3, v3
	v_lshl_add_u64 v[50:51], v[50:51], 0, v[70:71]
	global_store_dwordx2 v[50:51], v[16:17], off
	v_pk_mul_f32 v[16:17], v[88:89], v[14:15] op_sel_hi:[1,0]
	v_pk_mul_f32 v[54:55], v[90:91], v[14:15] op_sel_hi:[1,0]
	v_pk_mul_f32 v[16:17], v[6:7], v[16:17]
	v_pk_mul_f32 v[54:55], v[66:67], v[54:55]
	v_mul_f32_e32 v15, 0xbfb8aa3b, v17
	v_add_f32_e32 v3, 1.0, v3
	v_exp_f32_e32 v15, v15
	v_mul_f32_e32 v13, 0xbfb8aa3b, v55
	v_rcp_f32_e32 v3, v3
	v_exp_f32_e32 v13, v13
	v_pk_mul_f32 v[50:51], v[84:85], v[14:15] op_sel_hi:[1,0]
	v_add_f32_e32 v15, 1.0, v15
	v_mul_f32_e32 v3, v53, v3
	v_pk_mul_f32 v[50:51], v[68:69], v[50:51]
	v_add_f32_e32 v13, 1.0, v13
	v_mul_f32_e32 v3, v52, v3
	v_mul_f32_e32 v52, 0xbfb8aa3b, v51
	v_rcp_f32_e32 v13, v13
	v_exp_f32_e32 v52, v52
	v_rcp_f32_e32 v15, v15
	v_mul_f32_e32 v3, 0x41000000, v3
	v_mul_f32_e32 v13, v55, v13
	v_add_f32_e32 v52, 1.0, v52
	v_mul_f32_e32 v13, v54, v13
	v_rcp_f32_e32 v54, v52
	v_pk_mul_f32 v[52:53], v[82:83], v[14:15] op_sel_hi:[1,0]
	v_mul_f32_e32 v15, v17, v15
	v_pk_mul_f32 v[52:53], v[8:9], v[52:53]
	v_mul_f32_e32 v56, v16, v15
	v_mul_f32_e32 v55, 0xbfb8aa3b, v53
	v_exp_f32_e32 v55, v55
	v_mul_f32_e32 v15, v51, v54
	v_mul_f32_e32 v13, 0x41000000, v13
	v_med3_f32 v3, v3, s79, v206
	v_add_f32_e32 v16, 1.0, v55
	v_rcp_f32_e32 v51, v16
	v_pk_mul_f32 v[16:17], v[80:81], v[14:15] op_sel_hi:[1,0]
	v_mul_f32_e32 v55, v50, v15
	v_pk_mul_f32 v[16:17], v[38:39], v[16:17]
	v_mul_f32_e32 v15, v53, v51
	v_mul_f32_e32 v54, 0xbfb8aa3b, v17
	v_exp_f32_e32 v54, v54
	v_mul_f32_e32 v52, v52, v15
	v_med3_f32 v13, v13, s79, v206
	s_waitcnt vmcnt(7)
	v_mul_f32_e32 v12, v232, v233
	v_add_f32_e32 v15, 1.0, v54
	v_pk_mul_f32 v[50:51], v[78:79], v[14:15] op_sel_hi:[1,0]
	v_rcp_f32_e32 v53, v15
	v_pk_mul_f32 v[50:51], v[10:11], v[50:51]
	s_waitcnt vmcnt(5)
	v_mul_f32_e32 v2, v224, v225
	v_mul_f32_e32 v15, 0xbfb8aa3b, v51
	v_exp_f32_e32 v54, v15
	v_pk_mul_f32 v[14:15], v[76:77], v[14:15] op_sel_hi:[1,0]
	v_mul_f32_e32 v17, v17, v53
	v_pk_mul_f32 v[14:15], v[40:41], v[14:15]
	v_add_f32_e32 v53, 1.0, v54
	v_mul_f32_e32 v57, 0xbfb8aa3b, v15
	v_exp_f32_e32 v57, v57
	v_rcp_f32_e32 v53, v53
	v_mul_f32_e32 v16, v16, v17
	s_and_b64 vcc, exec, s[8:9]
	v_add_f32_e32 v54, 1.0, v57
	v_rcp_f32_e32 v54, v54
	v_mul_f32_e32 v17, v51, v53
	v_mul_f32_e32 v17, v50, v17
	s_mov_b64 s[8:9], -1
	v_mul_f32_e32 v15, v15, v54
	v_mul_f32_e32 v50, v14, v15
	v_mov_b32_e32 v14, 0
	v_cvt_pk_fp8_f32 v14, v3, v13
	v_mul_f32_e32 v15, 0x41000000, v56
	v_mul_f32_e32 v3, 0x41000000, v55
	v_med3_f32 v13, v15, s79, v206
	v_med3_f32 v3, v3, s79, v206
	v_cvt_pk_fp8_f32 v14, v13, v3 op_sel:[0,0,1]
	v_mul_f32_e32 v3, 0x41000000, v52
	v_mul_f32_e32 v13, 0x41000000, v16
	v_med3_f32 v3, v3, s79, v206
	v_med3_f32 v13, v13, s79, v206
	v_mov_b32_e32 v15, 0
	v_mul_f32_e32 v16, 0x41000000, v17
	v_cvt_pk_fp8_f32 v15, v3, v13
	v_med3_f32 v13, v16, s79, v206
	v_mul_f32_e32 v3, 0x41000000, v50
	v_pk_mul_f32 v[52:53], v[72:73], v[12:13] op_sel_hi:[1,0]
	v_med3_f32 v3, v3, s79, v206
	v_pk_mul_f32 v[52:53], v[66:67], v[52:53]
	v_cvt_pk_fp8_f32 v15, v13, v3 op_sel:[0,0,1]
	v_pk_mul_f32 v[50:51], v[74:75], v[12:13] op_sel_hi:[1,0]
	v_mul_f32_e32 v13, 0xbfb8aa3b, v53
	v_exp_f32_e32 v13, v13
	v_lshlrev_b64 v[16:17], 9, v[124:125]
	v_lshl_add_u64 v[16:17], s[2:3], 0, v[16:17]
	v_lshl_add_u64 v[16:17], v[16:17], 0, s[10:11]
	v_add_f32_e32 v13, 1.0, v13
	v_rcp_f32_e32 v13, v13
	v_lshl_add_u64 v[16:17], v[16:17], 0, s[30:31]
	v_lshl_add_u64 v[16:17], v[16:17], 0, v[70:71]
	global_store_dwordx2 v[16:17], v[14:15], off
	v_mul_f32_e32 v13, v53, v13
	v_pk_mul_f32 v[14:15], v[48:49], v[12:13] op_sel_hi:[1,0]
	v_pk_mul_f32 v[50:51], v[4:5], v[50:51]
	v_pk_mul_f32 v[14:15], v[6:7], v[14:15]
	v_mul_f32_e32 v3, 0xbfb8aa3b, v51
	v_mul_f32_e32 v16, 0xbfb8aa3b, v15
	v_exp_f32_e32 v48, v16
	v_pk_mul_f32 v[16:17], v[46:47], v[12:13] op_sel_hi:[1,0]
	v_mul_f32_e32 v47, v52, v13
	v_pk_mul_f32 v[16:17], v[68:69], v[16:17]
	v_add_f32_e32 v13, 1.0, v48
	v_rcp_f32_e32 v13, v13
	v_mul_f32_e32 v46, 0xbfb8aa3b, v17
	v_exp_f32_e32 v46, v46
	v_exp_f32_e32 v3, v3
	v_pk_mul_f32 v[44:45], v[44:45], v[12:13] op_sel_hi:[1,0]
	v_mul_f32_e32 v13, v15, v13
	v_pk_mul_f32 v[44:45], v[8:9], v[44:45]
	v_add_f32_e32 v46, 1.0, v46
	v_mul_f32_e32 v48, 0xbfb8aa3b, v45
	v_rcp_f32_e32 v46, v46
	v_exp_f32_e32 v48, v48
	v_mul_f32_e32 v49, v14, v13
	v_add_f32_e32 v3, 1.0, v3
	v_mul_f32_e32 v13, v17, v46
	v_add_f32_e32 v14, 1.0, v48
	v_rcp_f32_e32 v17, v14
	v_pk_mul_f32 v[14:15], v[42:43], v[12:13] op_sel_hi:[1,0]
	v_mul_f32_e32 v43, v16, v13
	v_pk_mul_f32 v[14:15], v[38:39], v[14:15]
	v_mul_f32_e32 v13, v45, v17
	v_mul_f32_e32 v42, 0xbfb8aa3b, v15
	v_exp_f32_e32 v42, v42
	v_mul_f32_e32 v44, v44, v13
	v_rcp_f32_e32 v3, v3
	v_add_f32_e32 v13, 1.0, v42
	v_pk_mul_f32 v[16:17], v[36:37], v[12:13] op_sel_hi:[1,0]
	v_rcp_f32_e32 v42, v13
	v_pk_mul_f32 v[16:17], v[10:11], v[16:17]
	v_mul_f32_e32 v3, v51, v3
	v_mul_f32_e32 v13, 0xbfb8aa3b, v17
	v_exp_f32_e32 v36, v13
	v_pk_mul_f32 v[12:13], v[34:35], v[12:13] op_sel_hi:[1,0]
	v_mul_f32_e32 v15, v15, v42
	v_pk_mul_f32 v[12:13], v[40:41], v[12:13]
	v_add_f32_e32 v35, 1.0, v36
	v_mul_f32_e32 v34, 0xbfb8aa3b, v13
	v_exp_f32_e32 v34, v34
	v_rcp_f32_e32 v35, v35
	v_mul_f32_e32 v3, v50, v3
	v_mul_f32_e32 v14, v14, v15
	v_add_f32_e32 v34, 1.0, v34
	v_rcp_f32_e32 v34, v34
	v_mul_f32_e32 v15, v17, v35
	v_mul_f32_e32 v15, v16, v15
	v_mul_f32_e32 v3, 0x41000000, v3
	v_mul_f32_e32 v13, v13, v34
	v_mul_f32_e32 v16, v12, v13
	v_mul_f32_e32 v12, 0x41000000, v47
	v_med3_f32 v3, v3, s79, v206
	v_med3_f32 v17, v12, s79, v206
	v_mov_b32_e32 v12, 0
	v_cvt_pk_fp8_f32 v12, v3, v17
	v_mul_f32_e32 v13, 0x41000000, v49
	v_mul_f32_e32 v3, 0x41000000, v43
	v_med3_f32 v13, v13, s79, v206
	v_med3_f32 v3, v3, s79, v206
	v_cvt_pk_fp8_f32 v12, v13, v3 op_sel:[0,0,1]
	v_mul_f32_e32 v3, 0x41000000, v44
	v_mul_f32_e32 v13, 0x41000000, v14
	v_mul_f32_e32 v14, 0x41000000, v15
	v_med3_f32 v3, v3, s79, v206
	v_med3_f32 v15, v13, s79, v206
	v_mov_b32_e32 v13, 0
	v_cvt_pk_fp8_f32 v13, v3, v15
	v_mul_f32_e32 v3, 0x41000000, v16
	v_med3_f32 v3, v3, s79, v206
	v_pk_mul_f32 v[16:17], v[32:33], v[2:3] op_sel_hi:[1,0]
	v_med3_f32 v14, v14, s79, v206
	v_pk_mul_f32 v[4:5], v[4:5], v[16:17]
	v_cvt_pk_fp8_f32 v13, v14, v3 op_sel:[0,0,1]
	v_mul_f32_e32 v3, 0xbfb8aa3b, v5
	v_exp_f32_e32 v3, v3
	v_lshlrev_b64 v[14:15], 9, v[96:97]
	v_lshl_add_u64 v[14:15], s[2:3], 0, v[14:15]
	v_lshl_add_u64 v[14:15], v[14:15], 0, s[10:11]
	v_pk_mul_f32 v[16:17], v[30:31], v[2:3] op_sel_hi:[1,0]
	v_add_f32_e32 v3, 1.0, v3
	v_pk_mul_f32 v[16:17], v[66:67], v[16:17]
	v_rcp_f32_e32 v3, v3
	v_mul_f32_e32 v30, 0xbfb8aa3b, v17
	v_exp_f32_e32 v30, v30
	v_lshl_add_u64 v[14:15], v[14:15], 0, s[30:31]
	v_lshl_add_u64 v[14:15], v[14:15], 0, v[70:71]
	v_mul_f32_e32 v3, v5, v3
	v_add_f32_e32 v30, 1.0, v30
	v_rcp_f32_e32 v30, v30
	global_store_dwordx2 v[14:15], v[12:13], off
	v_mul_f32_e32 v14, v4, v3
	v_mul_f32_e32 v3, v17, v30
	v_pk_mul_f32 v[4:5], v[28:29], v[2:3] op_sel_hi:[1,0]
	v_mul_f32_e32 v15, v16, v3
	v_pk_mul_f32 v[4:5], v[6:7], v[4:5]
	s_nop 0
	v_mul_f32_e32 v6, 0xbfb8aa3b, v5
	v_exp_f32_e32 v12, v6
	v_pk_mul_f32 v[6:7], v[26:27], v[2:3] op_sel_hi:[1,0]
	v_add_f32_e32 v3, 1.0, v12
	v_pk_mul_f32 v[6:7], v[68:69], v[6:7]
	v_rcp_f32_e32 v3, v3
	v_mul_f32_e32 v13, 0xbfb8aa3b, v7
	v_exp_f32_e32 v13, v13
	s_nop 0
	v_add_f32_e32 v12, 1.0, v13
	v_rcp_f32_e32 v16, v12
	v_pk_mul_f32 v[12:13], v[24:25], v[2:3] op_sel_hi:[1,0]
	v_mul_f32_e32 v3, v5, v3
	v_pk_mul_f32 v[8:9], v[8:9], v[12:13]
	v_mul_f32_e32 v13, v4, v3
	v_mul_f32_e32 v12, 0xbfb8aa3b, v9
	v_exp_f32_e32 v12, v12
	v_mul_f32_e32 v3, v7, v16
	v_mul_f32_e32 v16, v6, v3
	v_add_f32_e32 v4, 1.0, v12
	v_rcp_f32_e32 v7, v4
	v_pk_mul_f32 v[4:5], v[18:19], v[2:3] op_sel_hi:[1,0]
	v_mul_f32_e32 v3, v9, v7
	v_pk_mul_f32 v[4:5], v[38:39], v[4:5]
	v_mul_f32_e32 v8, v8, v3
	v_mul_f32_e32 v12, 0xbfb8aa3b, v5
	v_exp_f32_e32 v12, v12
	s_nop 0
	v_add_f32_e32 v3, 1.0, v12
	v_pk_mul_f32 v[6:7], v[22:23], v[2:3] op_sel_hi:[1,0]
	v_rcp_f32_e32 v9, v3
	v_pk_mul_f32 v[6:7], v[10:11], v[6:7]
	v_mul_f32_e32 v5, v5, v9
	v_mul_f32_e32 v3, 0xbfb8aa3b, v7
	v_exp_f32_e32 v10, v3
	v_pk_mul_f32 v[2:3], v[20:21], v[2:3] op_sel_hi:[1,0]
	v_mul_f32_e32 v4, v4, v5
	v_pk_mul_f32 v[2:3], v[40:41], v[2:3]
	v_add_f32_e32 v9, 1.0, v10
	v_mul_f32_e32 v11, 0xbfb8aa3b, v3
	v_exp_f32_e32 v11, v11
	v_rcp_f32_e32 v9, v9
	v_mul_f32_e32 v4, 0x41000000, v4
	v_med3_f32 v4, v4, s79, v206
	v_add_f32_e32 v10, 1.0, v11
	v_rcp_f32_e32 v10, v10
	v_mul_f32_e32 v5, v7, v9
	v_mul_f32_e32 v5, v6, v5
	v_mul_f32_e32 v7, 0x41000000, v13
	v_mul_f32_e32 v3, v3, v10
	v_mul_f32_e32 v6, v2, v3
	v_mul_f32_e32 v2, 0x41000000, v14
	v_mul_f32_e32 v3, 0x41000000, v15
	v_med3_f32 v9, v2, s79, v206
	v_med3_f32 v3, v3, s79, v206
	v_mov_b32_e32 v2, 0
	v_cvt_pk_fp8_f32 v2, v9, v3
	v_mul_f32_e32 v3, 0x41000000, v16
	v_med3_f32 v7, v7, s79, v206
	v_med3_f32 v3, v3, s79, v206
	v_cvt_pk_fp8_f32 v2, v7, v3 op_sel:[0,0,1]
	v_mul_f32_e32 v3, 0x41000000, v8
	v_med3_f32 v7, v3, s79, v206
	v_mov_b32_e32 v3, 0
	v_cvt_pk_fp8_f32 v3, v7, v4
	v_mul_f32_e32 v5, 0x41000000, v5
	v_mul_f32_e32 v4, 0x41000000, v6
	v_med3_f32 v5, v5, s79, v206
	v_med3_f32 v4, v4, s79, v206
	v_cvt_pk_fp8_f32 v3, v5, v4 op_sel:[0,0,1]
	v_lshlrev_b64 v[4:5], 9, v[94:95]
	v_lshl_add_u64 v[4:5], s[2:3], 0, v[4:5]
	v_lshl_add_u64 v[4:5], v[4:5], 0, s[10:11]
	v_lshl_add_u64 v[4:5], v[4:5], 0, s[30:31]
	v_lshl_add_u64 v[4:5], v[4:5], 0, v[70:71]
	global_store_dwordx2 v[4:5], v[2:3], off
	s_cbranch_vccnz .LBB0_1397
	s_andn2_b64 vcc, exec, s[34:35]
	s_cbranch_vccnz .LBB0_1396
	s_barrier
	s_branch .LBB0_1396

.LBB0_1505:
	s_lshl_b32 s2, s14, 8
	v_add_u32_e32 v248, s2, v169
	v_ashrrev_i32_e32 v249, 31, v248
	v_lshl_add_u64 v[248:249], v[248:249], 2, s[50:51]
	global_load_dword v240, v[248:249], off
	global_load_dword v241, v[248:249], off offset:64
	global_load_dword v242, v[248:249], off offset:128
	global_load_dword v243, v[248:249], off offset:192
	global_load_dword v244, v[248:249], off offset:512
	global_load_dword v245, v[248:249], off offset:576
	global_load_dword v246, v[248:249], off offset:640
	global_load_dword v247, v[248:249], off offset:704
	s_add_i32 s16, s16, 1
	s_and_b64 vcc, exec, s[8:9]
	s_mov_b64 s[62:63], s[94:95]
	s_mov_b64 s[12:13], s[52:53]
	s_cbranch_vccnz .LBB0_1514
	s_and_b64 vcc, exec, s[10:11]
	s_mov_b64 s[64:65], -1
	s_cbranch_vccnz .LBB0_1512
	s_add_i32 s2, s81, 2
	s_cmp_gt_u32 s2, 1
	s_mov_b64 s[62:63], -1
	s_cbranch_scc0 .LBB0_1509
	s_mul_i32 s2, s81, s29
	s_mul_hi_u32 s3, s81, s28
	s_add_i32 s3, s3, s2
	s_mul_i32 s2, s81, s28
	s_add_u32 s12, s2, s80
	s_addc_u32 s13, s3, s79
	s_mov_b64 s[62:63], 0

.LBB0_1520:
	v_mov_b32_e32 v2, 0
	s_lshl_b32 s2, s14, 8
	s_nop 15
	s_nop 15
	s_nop 15
	s_nop 15
	s_nop 15
	v_mov_b32_e32 v183, 0
	v_add3_u32 v184, s2, v169, v2
	v_ashrrev_i32_e32 v185, 31, v184
	v_lshl_add_u64 v[2:3], v[184:185], 2, s[50:51]
	v_mov_b32_e32 v192, v240
	v_add_u32_e32 v164, 16, v184
	v_add_u32_e32 v160, 48, v184
	v_add_u32_e32 v16, 0x80, v184
	v_add_u32_e32 v162, 32, v184
	v_add_u32_e32 v14, 0x90, v184
	v_add_u32_e32 v8, 0xa0, v184
	v_add_u32_e32 v4, 0xb0, v184
	v_ashrrev_i32_e32 v165, 31, v164
	v_ashrrev_i32_e32 v161, 31, v160
	v_ashrrev_i32_e32 v17, 31, v16
	v_ashrrev_i32_e32 v163, 31, v162
	v_ashrrev_i32_e32 v15, 31, v14
	v_ashrrev_i32_e32 v9, 31, v8
	v_ashrrev_i32_e32 v5, 31, v4
	v_lshl_add_u64 v[2:3], v[164:165], 2, s[50:51]
	v_lshl_add_u64 v[166:167], v[160:161], 2, s[50:51]
	v_lshl_add_u64 v[178:179], v[16:17], 2, s[50:51]
	v_lshl_add_u64 v[6:7], v[162:163], 2, s[50:51]
	v_lshl_add_u64 v[186:187], v[14:15], 2, s[50:51]
	v_lshl_add_u64 v[188:189], v[8:9], 2, s[50:51]
	v_lshl_add_u64 v[190:191], v[4:5], 2, s[50:51]
	v_mov_b32_e32 v182, v241
	v_mov_b32_e32 v181, v242
	v_mov_b32_e32 v180, v243
	s_nop 0
	v_mov_b32_e32 v179, v244
	s_nop 0
	v_mov_b32_e32 v178, v245
	v_mov_b32_e32 v167, v246
	v_mov_b32_e32 v166, v247
	s_lshl_b32 s2, s42, 8
	s_or_b32 s42, s2, s76
	v_mul_f32_e32 v6, 0x3a000000, v192
	v_pk_mul_f32 v[144:145], v[144:145], v[6:7] op_sel_hi:[1,0]
	v_pk_mul_f32 v[140:141], v[140:141], v[6:7] op_sel_hi:[1,0]
	v_pk_mul_f32 v[186:187], v[138:139], v[6:7] op_sel_hi:[1,0]
	v_pk_mul_f32 v[142:143], v[142:143], v[6:7] op_sel_hi:[1,0]
	v_max_f32_e64 v7, |v144|, |v145|
	v_max_f32_e64 v2, |v186|, |v187|
	v_max_f32_e64 v3, |v140|, |v141|
	v_max3_f32 v7, |v142|, |v143|, v7
	v_max3_f32 v3, v2, v3, v7
	ds_bpermute_b32 v7, v171, v3
	v_add_u32_e32 v138, v183, v168
	v_lshl_add_u32 v2, v138, 3, s42
	v_cmp_eq_u32_e64 s[14:15], 0, v138
	v_lshlrev_b64 v[138:139], 11, v[184:185]
	s_waitcnt lgkmcnt(0)
	v_max_f32_e32 v7, v7, v7
	v_max_f32_e32 v7, v3, v7
	ds_bpermute_b32 v183, v172, v7
	v_ashrrev_i32_e32 v3, 31, v2
	v_lshl_add_u64 v[138:139], s[54:55], 0, v[138:139]
	v_lshlrev_b64 v[184:185], 8, v[184:185]
	v_lshl_add_u64 v[138:139], v[138:139], 0, v[2:3]
	s_waitcnt lgkmcnt(0)
	v_max_f32_e32 v183, v183, v183
	v_max_f32_e32 v7, v7, v183
	v_div_scale_f32 v183, s[44:45], v7, v7, s17
	v_rcp_f32_e32 v188, v183
	v_div_scale_f32 v189, vcc, s17, v7, s17
	v_fma_f32 v190, -v183, v188, 1.0
	v_fmac_f32_e32 v188, v190, v188
	v_mul_f32_e32 v190, v189, v188
	v_fma_f32 v191, -v183, v190, v189
	v_fmac_f32_e32 v190, v191, v188
	v_fma_f32 v183, -v183, v190, v189
	v_div_fmas_f32 v183, v183, v188, v190
	v_div_fixup_f32 v183, v183, v7, s17
	v_cmp_lt_f32_e32 vcc, 0, v7
	s_nop 1
	v_cndmask_b32_e32 v183, 0, v183, vcc
	v_mul_f32_e32 v186, v186, v183
	v_mul_f32_e32 v187, v187, v183
	v_mul_f32_e32 v143, v143, v183
	v_mul_f32_e32 v140, v140, v183
	v_mul_f32_e32 v141, v141, v183
	v_mul_f32_e32 v142, v142, v183
	v_mul_f32_e32 v144, v144, v183
	v_mul_f32_e32 v145, v145, v183
	v_rndne_f32_e32 v183, v186
	v_rndne_f32_e32 v186, v187
	v_rndne_f32_e32 v143, v143
	v_rndne_f32_e32 v140, v140
	v_rndne_f32_e32 v141, v141
	v_rndne_f32_e32 v142, v142
	v_rndne_f32_e32 v144, v144
	v_rndne_f32_e32 v145, v145
	v_med3_f32 v186, v186, s84, v177
	v_med3_f32 v143, v143, s84, v177
	v_med3_f32 v183, v183, s84, v177
	v_med3_f32 v140, v140, s84, v177
	v_med3_f32 v141, v141, s84, v177
	v_med3_f32 v142, v142, s84, v177
	v_med3_f32 v144, v144, s84, v177
	v_med3_f32 v145, v145, s84, v177
	v_cvt_i32_f32_e32 v186, v186
	v_cvt_i32_f32_e32 v143, v143
	v_cvt_i32_f32_e32 v183, v183
	v_cvt_i32_f32_sdwa v140, v140 dst_sel:WORD_1 dst_unused:UNUSED_PAD src0_sel:DWORD
	v_cvt_i32_f32_e32 v141, v141
	v_cvt_i32_f32_e32 v142, v142
	v_cvt_i32_f32_sdwa v144, v144 dst_sel:WORD_1 dst_unused:UNUSED_PAD src0_sel:DWORD
	v_cvt_i32_f32_e32 v145, v145
	v_lshlrev_b32_e32 v186, 8, v186
	v_lshlrev_b32_e32 v143, 8, v143
	v_and_b32_e32 v140, 0xff0000, v140
	v_perm_b32 v141, v141, v183, s85
	v_and_b32_e32 v144, 0xff0000, v144
	v_perm_b32 v142, v145, v142, s85
	v_and_b32_e32 v145, 0xff00, v186
	v_and_b32_e32 v143, 0xff00, v143
	v_or3_b32 v140, v141, v145, v140
	v_or3_b32 v141, v142, v143, v144
	global_store_dwordx2 v[138:139], v[140:141], off
	v_lshl_add_u64 v[140:141], s[56:57], 0, v[184:185]
	s_and_saveexec_b64 s[66:67], s[14:15]
	s_cbranch_execz .LBB0_1522
	s_ashr_i32 s44, s42, 5
	s_ashr_i32 s45, s44, 31
	v_lshl_add_u64 v[142:143], s[44:45], 2, v[140:141]
	v_mul_f32_e32 v7, 0x3c010204, v7
	global_store_dword v[142:143], v7, off
